# speedup vs baseline: 1.0262x; 1.0179x over previous
.LBB2_54:
	s_or_b64 exec, exec, s[90:91]
	v_cmp_gt_u32_e32 vcc, 64, v0
	s_waitcnt lgkmcnt(0)
	s_barrier
	s_and_saveexec_b64 s[4:5], vcc
	s_cbranch_execz .LBB2_87
	v_mov_b32_e32 v2, 0x8800759c
	v_mov_b32_e32 v3, 0xfe37e43c
	v_bfrev_b32_e32 v6, -2
	v_mov_b32_e32 v153, v124
.Lmy_sel_loop:
	v_cmp_lt_i32_e32 vcc, v153, v127
	s_and_b64 exec, exec, vcc
	s_cbranch_execz .Lmy_sel_loop_end
	v_lshlrev_b32_e32 v154, 3, v153
	v_lshlrev_b32_e32 v155, 2, v153
	ds_read_b64 v[156:157], v154 offset:30208
	ds_read_b32 v158, v155 offset:13824
	v_add_u32_e32 v153, 64, v153
	s_waitcnt lgkmcnt(0)
	v_cmp_gt_f64_e64 s[8:9], v[156:157], v[2:3]
	v_cmp_eq_f64_e64 s[10:11], v[156:157], v[2:3]
	v_cmp_lt_i32_e64 s[12:13], v158, v6
	s_and_b64 s[10:11], s[10:11], s[12:13]
	s_or_b64 s[8:9], s[8:9], s[10:11]
	v_cndmask_b32_e64 v2, v2, v156, s[8:9]
	v_cndmask_b32_e64 v3, v3, v157, s[8:9]
	v_cndmask_b32_e64 v6, v6, v158, s[8:9]
	s_branch .Lmy_sel_loop
.Lmy_sel_loop_end:
	s_mov_b64 exec, -1
	s_nop 1
	v_mov_b32_dpp v156, v2 quad_perm:[1,0,3,2] row_mask:0xf bank_mask:0xf
	v_mov_b32_dpp v157, v3 quad_perm:[1,0,3,2] row_mask:0xf bank_mask:0xf
	v_mov_b32_dpp v158, v6 quad_perm:[1,0,3,2] row_mask:0xf bank_mask:0xf
	v_cmp_gt_f64_e64 s[8:9], v[156:157], v[2:3]
	v_cmp_eq_f64_e64 s[10:11], v[156:157], v[2:3]
	v_cmp_lt_i32_e64 s[12:13], v158, v6
	s_and_b64 s[10:11], s[10:11], s[12:13]
	s_or_b64 s[8:9], s[8:9], s[10:11]
	v_cndmask_b32_e64 v2, v2, v156, s[8:9]
	v_cndmask_b32_e64 v3, v3, v157, s[8:9]
	v_cndmask_b32_e64 v6, v6, v158, s[8:9]
	s_nop 1
	v_mov_b32_dpp v156, v2 quad_perm:[2,3,0,1] row_mask:0xf bank_mask:0xf
	v_mov_b32_dpp v157, v3 quad_perm:[2,3,0,1] row_mask:0xf bank_mask:0xf
	v_mov_b32_dpp v158, v6 quad_perm:[2,3,0,1] row_mask:0xf bank_mask:0xf
	v_cmp_gt_f64_e64 s[8:9], v[156:157], v[2:3]
	v_cmp_eq_f64_e64 s[10:11], v[156:157], v[2:3]
	v_cmp_lt_i32_e64 s[12:13], v158, v6
	s_and_b64 s[10:11], s[10:11], s[12:13]
	s_or_b64 s[8:9], s[8:9], s[10:11]
	v_cndmask_b32_e64 v2, v2, v156, s[8:9]
	v_cndmask_b32_e64 v3, v3, v157, s[8:9]
	v_cndmask_b32_e64 v6, v6, v158, s[8:9]
	s_nop 1
	v_mov_b32_dpp v156, v2 row_half_mirror row_mask:0xf bank_mask:0xf
	v_mov_b32_dpp v157, v3 row_half_mirror row_mask:0xf bank_mask:0xf
	v_mov_b32_dpp v158, v6 row_half_mirror row_mask:0xf bank_mask:0xf
	v_cmp_gt_f64_e64 s[8:9], v[156:157], v[2:3]
	v_cmp_eq_f64_e64 s[10:11], v[156:157], v[2:3]
	v_cmp_lt_i32_e64 s[12:13], v158, v6
	s_and_b64 s[10:11], s[10:11], s[12:13]
	s_or_b64 s[8:9], s[8:9], s[10:11]
	v_cndmask_b32_e64 v2, v2, v156, s[8:9]
	v_cndmask_b32_e64 v3, v3, v157, s[8:9]
	v_cndmask_b32_e64 v6, v6, v158, s[8:9]
	s_nop 1
	v_mov_b32_dpp v156, v2 row_mirror row_mask:0xf bank_mask:0xf
	v_mov_b32_dpp v157, v3 row_mirror row_mask:0xf bank_mask:0xf
	v_mov_b32_dpp v158, v6 row_mirror row_mask:0xf bank_mask:0xf
	v_cmp_gt_f64_e64 s[8:9], v[156:157], v[2:3]
	v_cmp_eq_f64_e64 s[10:11], v[156:157], v[2:3]
	v_cmp_lt_i32_e64 s[12:13], v158, v6
	s_and_b64 s[10:11], s[10:11], s[12:13]
	s_or_b64 s[8:9], s[8:9], s[10:11]
	v_cndmask_b32_e64 v2, v2, v156, s[8:9]
	v_cndmask_b32_e64 v3, v3, v157, s[8:9]
	v_cndmask_b32_e64 v6, v6, v158, s[8:9]
	ds_bpermute_b32 v156, v122, v2
	ds_bpermute_b32 v157, v122, v3
	ds_bpermute_b32 v158, v122, v6
	s_waitcnt lgkmcnt(0)
	v_cmp_gt_f64_e64 s[8:9], v[156:157], v[2:3]
	v_cmp_eq_f64_e64 s[10:11], v[156:157], v[2:3]
	v_cmp_lt_i32_e64 s[12:13], v158, v6
	s_and_b64 s[10:11], s[10:11], s[12:13]
	s_or_b64 s[8:9], s[8:9], s[10:11]
	v_cndmask_b32_e64 v2, v2, v156, s[8:9]
	v_cndmask_b32_e64 v3, v3, v157, s[8:9]
	v_cndmask_b32_e64 v6, v6, v158, s[8:9]
	ds_bpermute_b32 v156, v121, v2
	ds_bpermute_b32 v157, v121, v3
	ds_bpermute_b32 v158, v121, v6
	s_waitcnt lgkmcnt(0)
	v_cmp_gt_f64_e64 s[8:9], v[156:157], v[2:3]
	v_cmp_eq_f64_e64 s[10:11], v[156:157], v[2:3]
	v_cmp_lt_i32_e64 s[12:13], v158, v6
	s_and_b64 s[10:11], s[10:11], s[12:13]
	s_or_b64 s[8:9], s[8:9], s[10:11]
	v_cndmask_b32_e64 v2, v2, v156, s[8:9]
	v_cndmask_b32_e64 v3, v3, v157, s[8:9]
	v_cndmask_b32_e64 v6, v6, v158, s[8:9]
	s_and_b64 exec, exec, s[42:43]
	v_mov_b32_e32 v2, 0
	ds_write_b32 v2, v6 offset:65092

.LBB2_171:
	s_or_b64 exec, exec, s[2:3]
	v_cmp_lt_i32_e64 s[0:1], v97, v99
	s_waitcnt lgkmcnt(1)
	v_bfrev_b32_e32 v52, -2
	v_mov_b32_e32 v0, 0x8800759c
	v_mov_b32_e32 v1, 0xfe37e43c
	s_waitcnt lgkmcnt(0)
	s_barrier
	v_mov_b32_e32 v153, v97
	v_lshl_add_u32 v154, v97, 1, 0
	v_add_u32_e32 v155, 0x2b00, v100
.Lmy_f_loop:
	v_cmp_lt_i32_e64 s[6:7], v153, v99
	s_and_b64 exec, exec, s[6:7]
	s_cbranch_execz .Lmy_f_loop_end
	ds_read_u16 v156, v154
	ds_read_b64 v[158:159], v155
	v_add_u32_e32 v153, 16, v153
	v_add_u32_e32 v154, 32, v154
	v_add_u32_e32 v155, 0x80, v155
	s_waitcnt lgkmcnt(0)
	v_lshrrev_b32_e32 v157, 8, v156
	v_and_b32_e32 v156, 0xff, v156
	v_cmp_eq_u32_e64 s[2:3], v157, v98
	v_cmp_gt_f64_e64 s[8:9], v[158:159], v[0:1]
	v_cmp_eq_f64_e64 s[10:11], v[158:159], v[0:1]
	v_cmp_lt_u32_e64 s[12:13], v156, v52
	s_and_b64 s[10:11], s[10:11], s[12:13]
	s_or_b64 s[8:9], s[8:9], s[10:11]
	s_and_b64 s[8:9], s[8:9], s[2:3]
	v_cndmask_b32_e64 v0, v0, v158, s[8:9]
	v_cndmask_b32_e64 v1, v1, v159, s[8:9]
	v_cndmask_b32_e64 v52, v52, v156, s[8:9]
	s_branch .Lmy_f_loop
.Lmy_f_loop_end:
	s_mov_b64 exec, -1
	s_nop 1
	v_mov_b32_dpp v158, v0 quad_perm:[1,0,3,2] row_mask:0xf bank_mask:0xf
	v_mov_b32_dpp v159, v1 quad_perm:[1,0,3,2] row_mask:0xf bank_mask:0xf
	v_mov_b32_dpp v156, v52 quad_perm:[1,0,3,2] row_mask:0xf bank_mask:0xf
	v_cmp_gt_f64_e64 s[8:9], v[158:159], v[0:1]
	v_cmp_eq_f64_e64 s[10:11], v[158:159], v[0:1]
	v_cmp_lt_i32_e64 s[12:13], v156, v52
	s_and_b64 s[10:11], s[10:11], s[12:13]
	s_or_b64 s[8:9], s[8:9], s[10:11]
	v_cndmask_b32_e64 v0, v0, v158, s[8:9]
	v_cndmask_b32_e64 v1, v1, v159, s[8:9]
	v_cndmask_b32_e64 v52, v52, v156, s[8:9]
	s_nop 1
	v_mov_b32_dpp v158, v0 quad_perm:[2,3,0,1] row_mask:0xf bank_mask:0xf
	v_mov_b32_dpp v159, v1 quad_perm:[2,3,0,1] row_mask:0xf bank_mask:0xf
	v_mov_b32_dpp v156, v52 quad_perm:[2,3,0,1] row_mask:0xf bank_mask:0xf
	v_cmp_gt_f64_e64 s[8:9], v[158:159], v[0:1]
	v_cmp_eq_f64_e64 s[10:11], v[158:159], v[0:1]
	v_cmp_lt_i32_e64 s[12:13], v156, v52
	s_and_b64 s[10:11], s[10:11], s[12:13]
	s_or_b64 s[8:9], s[8:9], s[10:11]
	v_cndmask_b32_e64 v0, v0, v158, s[8:9]
	v_cndmask_b32_e64 v1, v1, v159, s[8:9]
	v_cndmask_b32_e64 v52, v52, v156, s[8:9]
	s_nop 1
	v_mov_b32_dpp v158, v0 row_half_mirror row_mask:0xf bank_mask:0xf
	v_mov_b32_dpp v159, v1 row_half_mirror row_mask:0xf bank_mask:0xf
	v_mov_b32_dpp v156, v52 row_half_mirror row_mask:0xf bank_mask:0xf
	v_cmp_gt_f64_e64 s[8:9], v[158:159], v[0:1]
	v_cmp_eq_f64_e64 s[10:11], v[158:159], v[0:1]
	v_cmp_lt_i32_e64 s[12:13], v156, v52
	s_and_b64 s[10:11], s[10:11], s[12:13]
	s_or_b64 s[8:9], s[8:9], s[10:11]
	v_cndmask_b32_e64 v0, v0, v158, s[8:9]
	v_cndmask_b32_e64 v1, v1, v159, s[8:9]
	v_cndmask_b32_e64 v52, v52, v156, s[8:9]
	s_nop 1
	v_mov_b32_dpp v158, v0 row_mirror row_mask:0xf bank_mask:0xf
	v_mov_b32_dpp v159, v1 row_mirror row_mask:0xf bank_mask:0xf
	v_mov_b32_dpp v156, v52 row_mirror row_mask:0xf bank_mask:0xf
	v_cmp_gt_f64_e64 s[8:9], v[158:159], v[0:1]
	v_cmp_eq_f64_e64 s[10:11], v[158:159], v[0:1]
	v_cmp_lt_i32_e64 s[12:13], v156, v52
	s_and_b64 s[10:11], s[10:11], s[12:13]
	s_or_b64 s[8:9], s[8:9], s[10:11]
	v_cndmask_b32_e64 v0, v0, v158, s[8:9]
	v_cndmask_b32_e64 v1, v1, v159, s[8:9]
	v_cndmask_b32_e64 v52, v52, v156, s[8:9]
	s_and_saveexec_b64 s[0:1], vcc
	s_cbranch_execz .LBB2_197

.LBB2_197:
	s_or_b64 exec, exec, s[0:1]
	v_lshlrev_b64 v[0:1], 3, v[86:87]
	v_lshl_add_u64 v[50:51], s[66:67], 0, v[0:1]
	v_lshl_add_u64 v[0:1], s[64:65], 0, v[0:1]
	s_waitcnt vmcnt(10)
	v_cvt_pk_f16_f32 v5, v4, v5
	v_cvt_pk_f16_f32 v4, v2, v3
	v_add_co_u32_e32 v2, vcc, 0x100000, v0
	v_cvt_pk_f16_f32 v9, v8, v9
	s_nop 0
	v_addc_co_u32_e32 v3, vcc, 0, v1, vcc
	global_store_dwordx2 v[2:3], v[4:5], off
	v_add_co_u32_e32 v4, vcc, 0x200000, v0
	s_waitcnt vmcnt(10)
	v_cvt_pk_f16_f32 v3, v16, v17
	v_cvt_pk_f16_f32 v2, v14, v15
	v_addc_co_u32_e32 v5, vcc, 0, v1, vcc
	global_store_dwordx2 v[4:5], v[2:3], off
	v_add_co_u32_e32 v4, vcc, 0x300000, v0
	s_waitcnt vmcnt(10)
	v_cvt_pk_f16_f32 v3, v12, v13
	v_cvt_pk_f16_f32 v2, v10, v11
	v_addc_co_u32_e32 v5, vcc, 0, v1, vcc
	global_store_dwordx2 v[4:5], v[2:3], off
	v_add_co_u32_e32 v4, vcc, 0x400000, v0
	s_waitcnt vmcnt(10)
	v_cvt_pk_f16_f32 v3, v24, v25
	v_cvt_pk_f16_f32 v2, v22, v23
	v_addc_co_u32_e32 v5, vcc, 0, v1, vcc
	global_store_dwordx2 v[4:5], v[2:3], off
	v_add_co_u32_e32 v4, vcc, 0x500000, v0
	s_waitcnt vmcnt(10)
	v_cvt_pk_f16_f32 v3, v20, v21
	v_cvt_pk_f16_f32 v2, v18, v19
	v_addc_co_u32_e32 v5, vcc, 0, v1, vcc
	global_store_dwordx2 v[4:5], v[2:3], off
	v_add_co_u32_e32 v4, vcc, 0x600000, v0
	v_cvt_pk_f16_f32 v8, v6, v7
	s_nop 0
	v_addc_co_u32_e32 v5, vcc, 0, v1, vcc
	global_store_dwordx2 v[0:1], v[8:9], off
	s_waitcnt vmcnt(11)
	v_cvt_pk_f16_f32 v3, v36, v37
	v_cvt_pk_f16_f32 v2, v34, v35
	v_add_co_u32_e32 v0, vcc, 0x700000, v0
	s_mov_b32 s0, 0x100000
	global_store_dwordx2 v[4:5], v[2:3], off
	s_waitcnt vmcnt(11)
	v_cvt_pk_f16_f32 v3, v28, v29
	v_cvt_pk_f16_f32 v2, v26, v27
	v_addc_co_u32_e32 v1, vcc, 0, v1, vcc
	global_store_dwordx2 v[0:1], v[2:3], off
	s_waitcnt vmcnt(11)
	v_cvt_pk_f16_f32 v1, v40, v41
	v_cvt_pk_f16_f32 v0, v38, v39
	v_add_co_u32_e32 v2, vcc, s0, v50
	s_mov_b32 s1, 0x200000
	global_store_dwordx2 v[50:51], v[0:1], off
	s_waitcnt vmcnt(11)
	v_cvt_pk_f16_f32 v1, v32, v33
	v_cvt_pk_f16_f32 v0, v30, v31
	v_addc_co_u32_e32 v3, vcc, 0, v51, vcc
	global_store_dwordx2 v[2:3], v[0:1], off
	v_add_co_u32_e32 v2, vcc, s1, v50
	s_waitcnt vmcnt(11)
	v_cvt_pk_f16_f32 v1, v48, v49
	v_cvt_pk_f16_f32 v0, v46, v47
	v_addc_co_u32_e32 v3, vcc, 0, v51, vcc
	global_store_dwordx2 v[2:3], v[0:1], off
	v_add_co_u32_e32 v2, vcc, 0x300000, v50
	s_waitcnt vmcnt(11)
	v_cvt_pk_f16_f32 v1, v44, v45
	v_cvt_pk_f16_f32 v0, v42, v43
	v_addc_co_u32_e32 v3, vcc, 0, v51, vcc
	global_store_dwordx2 v[2:3], v[0:1], off
	s_endpgm
	.section	.rodata,"a",@progbits
	.p2align	6, 0x0
